# speedup vs baseline: 1.0040x; 1.0040x over previous
_Z7k_finalPKfS0_Pf:
	s_load_dwordx4 s[4:7], s[0:1], 0x0
	s_load_dwordx2 s[8:9], s[0:1], 0x10
	s_lshl_b32 s0, s2, 8
	v_or_b32_e32 v4, s0, v0
	v_ashrrev_i32_e32 v5, 31, v4
	v_lshlrev_b64 v[0:1], 5, v[4:5]
	s_bfe_i32 s0, s2, 0x10017
	s_waitcnt lgkmcnt(0)
	v_lshl_add_u64 v[6:7], s[4:5], 0, v[0:1]
	s_lshr_b32 s0, s0, 18
	global_load_dwordx4 v[12:15], v[6:7], off
	global_load_dwordx4 v[0:3], v[6:7], off offset:16
	v_add_u32_e32 v6, s0, v4
	v_ashrrev_i32_e32 v6, 14, v6
	v_ashrrev_i32_e32 v7, 31, v6
	v_lshl_add_u64 v[6:7], v[6:7], 2, s[6:7]
	global_load_dword v10, v[6:7], off
	s_waitcnt vmcnt(2)
	v_mov_b32_e32 v6, v12
	s_waitcnt vmcnt(1)
	v_mov_b32_e32 v7, v0
	v_mov_b32_e32 v0, v13
	v_mov_b32_e32 v8, v14
	v_mov_b32_e32 v9, v2
	v_mov_b32_e32 v2, v15
	v_pk_add_f32 v[0:1], v[6:7], v[0:1]
	v_pk_add_f32 v[2:3], v[8:9], v[2:3]
	s_nop 0
	v_pk_add_f32 v[0:1], v[0:1], v[2:3]
	s_nop 0
	v_add_f32_e32 v0, v0, v1
	s_waitcnt vmcnt(0)
	v_add_f32_e32 v0, v10, v0
	v_mul_f32_e32 v0, 0xbfb8aa3b, v0
	v_exp_f32_e32 v0, v0
	s_nop 0
	v_add_f32_e32 v0, 1.0, v0
	v_div_scale_f32 v1, s[0:1], v0, v0, 1.0
	v_rcp_f32_e32 v2, v1
	v_div_scale_f32 v3, vcc, 1.0, v0, 1.0
	v_fma_f32 v6, -v1, v2, 1.0
	v_fmac_f32_e32 v2, v6, v2
	v_mul_f32_e32 v6, v3, v2
	v_fma_f32 v7, -v1, v6, v3
	v_fmac_f32_e32 v6, v7, v2
	v_fma_f32 v1, -v1, v6, v3
	v_div_fmas_f32 v1, v1, v2, v6
	v_div_fixup_f32 v2, v1, v0, 1.0
	v_lshl_add_u64 v[0:1], v[4:5], 2, s[8:9]
	global_store_dword v[0:1], v2, off
	s_nop 0
	s_endpgm

.LBB4_20:
	s_endpgm
	.p2alignl 8, 3212836864

.LBB6_38:
	s_barrier
	s_endpgm
	.p2alignl 8, 3212836864

	.text
	.p2alignl 6, 3212836864
	.fill 256, 4, 3212836864
	.p2alignl 8, 3212836864
